# speedup vs baseline: 1.0095x; 1.0095x over previous
_Z11attn_kernel8AttnArgs:
	v_readfirstlane_b32 s3, v0
	s_nop 3
	s_lshr_b32 s3, s3, 8
	s_cmp_eq_u32 s3, 0
	s_cbranch_scc1 .Lattn_prio_done
	s_setprio 1
.Lattn_prio_done:
	s_load_dwordx16 s[12:27], s[0:1], 0x0
	s_load_dwordx4 s[28:31], s[0:1], 0xa0
	s_load_dwordx8 s[36:43], s[0:1], 0x80
	s_load_dwordx2 s[34:35], s[0:1], 0xd0
	s_load_dwordx8 s[44:51], s[0:1], 0xb0
	s_and_b32 s3, s2, 0xff
	s_xor_b32 s58, s3, 0x80
	s_cmpk_gt_u32 s58, 0x7f
	s_cselect_b64 s[8:9], -1, 0
	s_and_b64 vcc, exec, s[8:9]
	s_cbranch_vccnz .LBB1_2
	s_cbranch_execz .LBB1_3
	s_branch .LBB1_22
